# out-proj GEMM epilogue: bf16 residual pieces loaded and output rows stored as lane-contiguous 16-byte accesses through a per-wave LDS tile (misc LDS area) instead of one-row-per-lane 8-byte accesses
# speedup vs baseline: 1.0345x; 1.0068x over previous
;     __device__ __forceinline__ void operator()(const f32x4 (&acc)[2][2][4][2], const Unit& u, int wr, int wc, int fr, int fq) const {
;         const int row0 = u.pm * BM + wr * 64 + fr, col0 = u.pn * BM + wc * 32 + 4 * fq;
; #pragma unroll
;         for (int ai = 0; ai < 2; ++ai)
; #pragma unroll
;             for (int m = 0; m < 4; ++m) { const int row = row0 + ai * HALF + m * 16; const size_t ro = (size_t)row * 2048 + col0;
;                 float s = 0.f;
; #pragma unroll
;                 for (int bj = 0; bj < 2; ++bj)
; #pragma unroll
;                     for (int n = 0; n < 2; ++n) { f32x4 r;
;                         if (R32) r = *(const f32x4*)(R32 + ro + bj * HALF + n * 16);
;                         else { typedef unsigned u32x2_t __attribute__((ext_vector_type(2))); const u32x2_t rw = *(const u32x2_t*)(R16 + ro + bj * HALF + n * 16); const unsigned r0 = rw.x, r1 = rw.y;
;                             r = (f32x4){__builtin_bit_cast(float, r0 << 16), __builtin_bit_cast(float, r0 & 0xffff0000u), __builtin_bit_cast(float, r1 << 16), __builtin_bit_cast(float, r1 & 0xffff0000u)}; }
.LBB0_728:
	v_and_b32_e32 v180, 15, v211
	v_lshrrev_b32_e32 v181, 4, v211
	v_lshrrev_b32_e32 v182, 3, v211
	v_bfe_u32 v183, v211, 2, 1
	v_lshrrev_b32_e32 v234, 6, v212
	v_mul_u32_u24_e32 v234, 0xc00, v234
	v_add_u32_e32 v234, 0x20400, v234
	v_mul_u32_u24_e32 v235, 0x90, v182
	v_add_u32_e32 v235, v234, v235
	v_lshl_add_u32 v235, v183, 6, v235
	v_and_b32_e32 v236, 3, v211
	v_lshl_add_u32 v235, v236, 4, v235
	v_mul_u32_u24_e32 v237, 0x90, v180
	v_add_u32_e32 v234, v234, v237
	v_lshl_add_u32 v234, v181, 3, v234
	v_sub_u32_e32 v237, v182, v180
	v_lshlrev_b32_e32 v237, 12, v237
	v_lshl_add_u32 v237, v183, 8, v237
	v_lshl_add_u32 v237, v236, 4, v237
	v_lshlrev_b32_e32 v236, 3, v181
	v_sub_u32_e32 v236, v237, v236
	v_ashrrev_i32_e32 v237, 31, v236
	v_mov_b32_e32 v206, 0x8000
	v_mov_b32_e32 v207, 0
	v_lshl_add_u32 v138, s40, 8, v152
	v_lshl_or_b32 v142, s64, 8, v154
	v_ashrrev_i32_e32 v139, 31, v138
	v_ashrrev_i32_e32 v143, 31, v142
	v_lshlrev_b64 v[128:129], 11, v[138:139]
	v_readlane_b32 s4, v252, 2
	v_lshl_add_u64 v[140:141], v[128:129], 0, v[142:143]
	v_cndmask_b32_e64 v128, 0, 1, s[88:89]
	v_readlane_b32 s5, v252, 3
	s_mov_b64 s[2:3], -1
	v_cmp_ne_u32_e64 s[40:41], 1, v128
	s_andn2_b64 vcc, exec, s[88:89]
	v_lshl_add_u64 v[144:145], v[140:141], 2, s[4:5]
	v_readlane_b32 s58, v250, 24
	v_readlane_b32 s68, v250, 25
	v_readlane_b32 s66, v250, 30
	v_readlane_b32 s6, v252, 4
	v_readlane_b32 s7, v252, 5
	v_readlane_b32 s8, v252, 6
	v_readlane_b32 s9, v252, 7
	v_readlane_b32 s10, v252, 8
	v_readlane_b32 s11, v252, 9
	v_readlane_b32 s12, v252, 10
	v_readlane_b32 s13, v252, 11
	v_readlane_b32 s14, v252, 12
	v_readlane_b32 s15, v252, 13
	v_readlane_b32 s16, v252, 14
	v_readlane_b32 s17, v252, 15
	v_readlane_b32 s18, v252, 16
	v_readlane_b32 s19, v252, 17
	s_cbranch_vccnz .LBB0_730
	global_load_dwordx4 v[128:131], v[144:145], off
	s_waitcnt vmcnt(0)
	s_mov_b64 s[2:3], 0
.LBB0_730:
	s_andn2_b64 vcc, exec, s[2:3]
	v_lshl_add_u64 v[146:147], v[140:141], 1, s[48:49]
	s_cbranch_vccnz .LBB0_732
	v_mov_b32_e32 v204, v146
	v_mov_b32_e32 v205, v147
	v_lshl_add_u64 v[208:209], v[204:205], 0, v[236:237]
	global_load_dwordx4 v[156:159], v[208:209], off
	v_lshl_add_u64 v[208:209], v[208:209], 0, v[206:207]
	global_load_dwordx4 v[160:163], v[208:209], off
	s_mov_b32 s100, 0x10000
	s_mov_b32 s101, 0
	v_lshl_add_u64 v[202:203], v[204:205], 0, s[100:101]
	v_lshl_add_u64 v[208:209], v[202:203], 0, v[236:237]
	global_load_dwordx4 v[164:167], v[208:209], off
	v_lshl_add_u64 v[208:209], v[208:209], 0, v[206:207]
	global_load_dwordx4 v[168:171], v[208:209], off
	s_mov_b32 s100, 0x20000
	s_mov_b32 s101, 0
	v_lshl_add_u64 v[202:203], v[204:205], 0, s[100:101]
	v_lshl_add_u64 v[208:209], v[202:203], 0, v[236:237]
	global_load_dwordx4 v[172:175], v[208:209], off
	v_lshl_add_u64 v[208:209], v[208:209], 0, v[206:207]
	global_load_dwordx4 v[176:179], v[208:209], off
	s_mov_b32 s100, 0x30000
	s_mov_b32 s101, 0
	v_lshl_add_u64 v[202:203], v[204:205], 0, s[100:101]
	v_lshl_add_u64 v[208:209], v[202:203], 0, v[236:237]
	global_load_dwordx4 v[194:197], v[208:209], off
	v_lshl_add_u64 v[208:209], v[208:209], 0, v[206:207]
	global_load_dwordx4 v[198:201], v[208:209], off
	s_waitcnt vmcnt(6)
	ds_write_b128 v235, v[156:159]
	ds_write_b128 v235, v[160:163] offset:1152
	s_waitcnt lgkmcnt(0)
	ds_read_b64 v[226:227], v234
	ds_read_b64 v[228:229], v234 offset:32
	ds_read_b64 v[230:231], v234 offset:64
	ds_read_b64 v[232:233], v234 offset:96
	s_waitcnt lgkmcnt(0)
	v_lshlrev_b32_e32 v128, 16, v226
	v_and_b32_e32 v129, 0xffff0000, v226
	v_lshlrev_b32_e32 v130, 16, v227
	v_and_b32_e32 v131, 0xffff0000, v227
; __device__ __forceinline__ unsigned cvt_pk_bf16(float lo, float hi) { unsigned r; asm volatile("v_cvt_pk_bf16_f32 %0, %1, %2" : "=v"(r) : "v"(lo), "v"(hi)); return r; }
;     __device__ __forceinline__ void operator()(const f32x4 (&acc)[2][2][4][2], const Unit& u, int wr, int wc, int fr, int fq) const {
;     ...
;                         if (R32) r = *(const f32x4*)(R32 + ro + bj * HALF + n * 16);
;                         else { typedef unsigned u32x2_t __attribute__((ext_vector_type(2))); const u32x2_t rw = *(const u32x2_t*)(R16 + ro + bj * HALF + n * 16); const unsigned r0 = rw.x, r1 = rw.y;
;                             r = (f32x4){__builtin_bit_cast(float, r0 << 16), __builtin_bit_cast(float, r0 & 0xffff0000u), __builtin_bit_cast(float, r1 << 16), __builtin_bit_cast(float, r1 & 0xffff0000u)}; }
;                         const f32x4 v = acc[ai][bj][m][n] + r;
;                         typedef unsigned u32x2_s __attribute__((ext_vector_type(2))); u32x2_s w; w.x = cvt_pk_bf16(v[0], v[1]); w.y = cvt_pk_bf16(v[2], v[3]);
;                         *(u32x2_s*)(XB + ro + bj * HALF + n * 16) = w;
;                         s += (v[0] * v[0] + v[1] * v[1]) + (v[2] * v[2] + v[3] * v[3]); }
;                 s += __shfl_xor(s, 16); s += __shfl_xor(s, 32);
;                 if (fq == 0) ss2[(size_t)(u.pn * 4 + wc) * MT + row] = s; }
.LBB0_732:
	v_pk_add_f32 v[130:131], v[126:127], v[130:131]
	v_pk_add_f32 v[148:149], v[124:125], v[128:129]
	v_lshl_add_u64 v[128:129], v[140:141], 1, s[90:91]
	v_cvt_pk_bf16_f32 v124, v148, v149
	v_cvt_pk_bf16_f32 v125, v130, v131
	s_and_b64 vcc, exec, s[40:41]
	s_mov_b64 s[2:3], -1
	ds_write_b64 v234, v[124:125]
	s_cbranch_vccnz .LBB0_734
	global_load_dwordx4 v[124:127], v[144:145], off offset:64
	s_waitcnt vmcnt(0)
	s_mov_b64 s[2:3], 0
.LBB0_734:
	s_andn2_b64 vcc, exec, s[2:3]
	s_cbranch_vccnz .LBB0_736
	v_lshlrev_b32_e32 v124, 16, v228
	v_and_b32_e32 v125, 0xffff0000, v228
	v_lshlrev_b32_e32 v126, 16, v229
	v_and_b32_e32 v127, 0xffff0000, v229
.LBB0_736:
	v_pk_add_f32 v[126:127], v[122:123], v[126:127]
	v_pk_add_f32 v[124:125], v[120:121], v[124:125]
	s_and_b64 vcc, exec, s[40:41]
	v_cvt_pk_bf16_f32 v120, v124, v125
	v_cvt_pk_bf16_f32 v121, v126, v127
	s_mov_b64 s[2:3], -1
	ds_write_b64 v234, v[120:121] offset:32
	s_cbranch_vccnz .LBB0_738
	global_load_dwordx4 v[120:123], v[144:145], off offset:512
	s_waitcnt vmcnt(0)
	s_mov_b64 s[2:3], 0
.LBB0_738:
	s_andn2_b64 vcc, exec, s[2:3]
	s_cbranch_vccnz .LBB0_740
	v_lshlrev_b32_e32 v120, 16, v230
	v_and_b32_e32 v121, 0xffff0000, v230
	v_lshlrev_b32_e32 v122, 16, v231
	v_and_b32_e32 v123, 0xffff0000, v231
.LBB0_740:
	v_pk_add_f32 v[122:123], v[118:119], v[122:123]
	v_pk_add_f32 v[120:121], v[116:117], v[120:121]
	s_and_b64 vcc, exec, s[40:41]
	v_cvt_pk_bf16_f32 v116, v120, v121
	v_cvt_pk_bf16_f32 v117, v122, v123
	s_mov_b64 s[2:3], -1
	ds_write_b64 v234, v[116:117] offset:64
	s_cbranch_vccnz .LBB0_742
	global_load_dwordx4 v[116:119], v[144:145], off offset:576
	s_waitcnt vmcnt(0)
	s_mov_b64 s[2:3], 0
.LBB0_742:
	s_andn2_b64 vcc, exec, s[2:3]
	s_cbranch_vccnz .LBB0_744
	v_lshlrev_b32_e32 v116, 16, v232
	v_and_b32_e32 v117, 0xffff0000, v232
	v_lshlrev_b32_e32 v118, 16, v233
	v_and_b32_e32 v119, 0xffff0000, v233
.LBB0_744:
	v_mul_f32_e32 v125, v125, v125
	v_mul_f32_e32 v144, v149, v149
	v_mul_f32_e32 v131, v131, v131
	v_fmac_f32_e32 v125, v124, v124
	v_mul_f32_e32 v124, v127, v127
	v_mul_f32_e32 v121, v121, v121
	v_fmac_f32_e32 v144, v148, v148
	v_fmac_f32_e32 v131, v130, v130
	v_fmac_f32_e32 v124, v126, v126
	v_fmac_f32_e32 v121, v120, v120
	v_mul_f32_e32 v120, v123, v123
	v_pk_add_f32 v[114:115], v[114:115], v[118:119]
	v_pk_add_f32 v[116:117], v[112:113], v[116:117]
	v_add_f32_e32 v130, v144, v131
	v_add_f32_e32 v124, v125, v124
	v_fmac_f32_e32 v120, v122, v122
	v_mul_f32_e32 v112, v117, v117
	v_mul_f32_e32 v113, v115, v115
	v_add_f32_e32 v124, v130, v124
	v_add_f32_e32 v120, v121, v120
	v_fmac_f32_e32 v112, v116, v116
	v_fmac_f32_e32 v113, v114, v114
	v_add_f32_e32 v120, v124, v120
	v_add_f32_e32 v112, v112, v113
	v_add_f32_e32 v112, v120, v112
	ds_bpermute_b32 v113, v150, v112
	s_lshl_b32 s2, s64, 2
	s_or_b32 s2, s2, s53
	s_ashr_i32 s3, s2, 31
	s_lshl_b64 s[24:25], s[2:3], 16
	s_waitcnt lgkmcnt(0)
	v_add_f32_e32 v112, v112, v113
	ds_bpermute_b32 v113, v151, v112
	v_cvt_pk_bf16_f32 v116, v116, v117
	v_cvt_pk_bf16_f32 v117, v114, v115
	ds_write_b64 v234, v[116:117] offset:96
	s_waitcnt lgkmcnt(0)
	ds_read_b128 v[226:229], v235
	ds_read_b128 v[230:233], v235 offset:1152
	v_lshl_add_u64 v[238:239], v[128:129], 0, v[236:237]
	s_waitcnt lgkmcnt(1)
	global_store_dwordx4 v[238:239], v[226:229], off
	v_lshl_add_u64 v[238:239], v[238:239], 0, v[206:207]
	s_waitcnt lgkmcnt(0)
	global_store_dwordx4 v[238:239], v[230:233], off
	s_and_saveexec_b64 s[2:3], s[36:37]
	s_cbranch_execz .LBB0_746
	v_readlane_b32 s4, v250, 32
	v_readlane_b32 s5, v250, 33
	s_add_u32 s4, s4, s24
	s_addc_u32 s5, s5, s25
	v_lshl_add_u64 v[114:115], v[138:139], 2, s[4:5]
	s_waitcnt lgkmcnt(0)
	v_add_f32_e32 v112, v112, v113
	global_store_dword v[114:115], v112, off

; __device__ __forceinline__ unsigned cvt_pk_bf16(float lo, float hi) { unsigned r; asm volatile("v_cvt_pk_bf16_f32 %0, %1, %2" : "=v"(r) : "v"(lo), "v"(hi)); return r; }
;     __device__ __forceinline__ void operator()(const f32x4 (&acc)[2][2][4][2], const Unit& u, int wr, int wc, int fr, int fq) const {
;     ...
;                         if (R32) r = *(const f32x4*)(R32 + ro + bj * HALF + n * 16);
;                         else { typedef unsigned u32x2_t __attribute__((ext_vector_type(2))); const u32x2_t rw = *(const u32x2_t*)(R16 + ro + bj * HALF + n * 16); const unsigned r0 = rw.x, r1 = rw.y;
;                             r = (f32x4){__builtin_bit_cast(float, r0 << 16), __builtin_bit_cast(float, r0 & 0xffff0000u), __builtin_bit_cast(float, r1 << 16), __builtin_bit_cast(float, r1 & 0xffff0000u)}; }
;                         const f32x4 v = acc[ai][bj][m][n] + r;
;                         typedef unsigned u32x2_s __attribute__((ext_vector_type(2))); u32x2_s w; w.x = cvt_pk_bf16(v[0], v[1]); w.y = cvt_pk_bf16(v[2], v[3]);
;                         *(u32x2_s*)(XB + ro + bj * HALF + n * 16) = w;
;                         s += (v[0] * v[0] + v[1] * v[1]) + (v[2] * v[2] + v[3] * v[3]); }
;                 s += __shfl_xor(s, 16); s += __shfl_xor(s, 32);
;                 if (fq == 0) ss2[(size_t)(u.pn * 4 + wc) * MT + row] = s; }
.LBB0_748:
	s_andn2_b64 vcc, exec, s[2:3]
	v_lshl_add_u64 v[118:119], v[122:123], 1, s[48:49]
	s_cbranch_vccnz .LBB0_750
	s_mov_b32 s100, 0x80000
	s_mov_b32 s101, 0
	v_lshl_add_u64 v[202:203], v[204:205], 0, s[100:101]
	v_lshl_add_u64 v[208:209], v[202:203], 0, v[236:237]
	global_load_dwordx4 v[156:159], v[208:209], off
	v_lshl_add_u64 v[208:209], v[208:209], 0, v[206:207]
	global_load_dwordx4 v[160:163], v[208:209], off
	s_waitcnt vmcnt(8)
	ds_write_b128 v235, v[164:167]
	ds_write_b128 v235, v[168:171] offset:1152
	s_waitcnt lgkmcnt(0)
	ds_read_b64 v[226:227], v234
	ds_read_b64 v[228:229], v234 offset:32
	ds_read_b64 v[230:231], v234 offset:64
	ds_read_b64 v[232:233], v234 offset:96
	s_waitcnt lgkmcnt(0)
	v_lshlrev_b32_e32 v112, 16, v226
	v_and_b32_e32 v113, 0xffff0000, v226
	v_lshlrev_b32_e32 v114, 16, v227
	v_and_b32_e32 v115, 0xffff0000, v227
.LBB0_750:
	v_pk_add_f32 v[114:115], v[110:111], v[114:115]
	v_pk_add_f32 v[120:121], v[108:109], v[112:113]
	v_lshl_add_u64 v[112:113], v[122:123], 1, s[90:91]
	v_cvt_pk_bf16_f32 v108, v120, v121
	v_cvt_pk_bf16_f32 v109, v114, v115
	s_and_b64 vcc, exec, s[40:41]
	s_mov_b64 s[2:3], -1
	ds_write_b64 v234, v[108:109]
	s_cbranch_vccnz .LBB0_752
	global_load_dwordx4 v[108:111], v[116:117], off offset:64
	s_waitcnt vmcnt(0)
	s_mov_b64 s[2:3], 0
.LBB0_752:
	s_andn2_b64 vcc, exec, s[2:3]
	s_cbranch_vccnz .LBB0_754
	v_lshlrev_b32_e32 v108, 16, v228
	v_and_b32_e32 v109, 0xffff0000, v228
	v_lshlrev_b32_e32 v110, 16, v229
	v_and_b32_e32 v111, 0xffff0000, v229
.LBB0_754:
	v_pk_add_f32 v[110:111], v[106:107], v[110:111]
	v_pk_add_f32 v[108:109], v[104:105], v[108:109]
	s_and_b64 vcc, exec, s[40:41]
	v_cvt_pk_bf16_f32 v104, v108, v109
	v_cvt_pk_bf16_f32 v105, v110, v111
	s_mov_b64 s[2:3], -1
	ds_write_b64 v234, v[104:105] offset:32
	s_cbranch_vccnz .LBB0_756
	global_load_dwordx4 v[104:107], v[116:117], off offset:512
	s_waitcnt vmcnt(0)
	s_mov_b64 s[2:3], 0
.LBB0_756:
	s_andn2_b64 vcc, exec, s[2:3]
	s_cbranch_vccnz .LBB0_758
	v_lshlrev_b32_e32 v104, 16, v230
	v_and_b32_e32 v105, 0xffff0000, v230
	v_lshlrev_b32_e32 v106, 16, v231
	v_and_b32_e32 v107, 0xffff0000, v231
.LBB0_758:
	v_pk_add_f32 v[106:107], v[102:103], v[106:107]
	v_pk_add_f32 v[104:105], v[100:101], v[104:105]
	s_and_b64 vcc, exec, s[40:41]
	v_cvt_pk_bf16_f32 v100, v104, v105
	v_cvt_pk_bf16_f32 v101, v106, v107
	s_mov_b64 s[2:3], -1
	ds_write_b64 v234, v[100:101] offset:64
	s_cbranch_vccnz .LBB0_760
	global_load_dwordx4 v[100:103], v[116:117], off offset:576
	s_waitcnt vmcnt(0)
	s_mov_b64 s[2:3], 0
.LBB0_760:
	s_andn2_b64 vcc, exec, s[2:3]
	s_cbranch_vccnz .LBB0_762
	v_lshlrev_b32_e32 v100, 16, v232
	v_and_b32_e32 v101, 0xffff0000, v232
	v_lshlrev_b32_e32 v102, 16, v233
	v_and_b32_e32 v103, 0xffff0000, v233
.LBB0_762:
	v_mul_f32_e32 v109, v109, v109
	v_mul_f32_e32 v116, v121, v121
	v_mul_f32_e32 v115, v115, v115
	v_fmac_f32_e32 v109, v108, v108
	v_mul_f32_e32 v108, v111, v111
	v_mul_f32_e32 v105, v105, v105
	v_fmac_f32_e32 v116, v120, v120
	v_fmac_f32_e32 v115, v114, v114
	v_fmac_f32_e32 v108, v110, v110
	v_fmac_f32_e32 v105, v104, v104
	v_mul_f32_e32 v104, v107, v107
	v_pk_add_f32 v[98:99], v[98:99], v[102:103]
	v_pk_add_f32 v[100:101], v[96:97], v[100:101]
	v_add_f32_e32 v114, v116, v115
	v_add_f32_e32 v108, v109, v108
	v_fmac_f32_e32 v104, v106, v106
	v_mul_f32_e32 v96, v101, v101
	v_mul_f32_e32 v97, v99, v99
	v_add_f32_e32 v108, v114, v108
	v_add_f32_e32 v104, v105, v104
	v_fmac_f32_e32 v96, v100, v100
	v_fmac_f32_e32 v97, v98, v98
	v_add_f32_e32 v104, v108, v104
	v_add_f32_e32 v96, v96, v97
	v_add_f32_e32 v96, v104, v96
	ds_bpermute_b32 v97, v150, v96
	v_cvt_pk_bf16_f32 v100, v100, v101
	v_cvt_pk_bf16_f32 v101, v98, v99
	ds_write_b64 v234, v[100:101] offset:96
	s_waitcnt lgkmcnt(0)
	ds_read_b128 v[226:229], v235
	ds_read_b128 v[230:233], v235 offset:1152
	v_lshl_add_u64 v[238:239], v[112:113], 0, v[236:237]
	s_waitcnt lgkmcnt(1)
	global_store_dwordx4 v[238:239], v[226:229], off
	v_lshl_add_u64 v[238:239], v[238:239], 0, v[206:207]
	s_waitcnt lgkmcnt(0)
	global_store_dwordx4 v[238:239], v[230:233], off
	s_waitcnt lgkmcnt(0)
	v_add_f32_e32 v96, v96, v97
	ds_bpermute_b32 v97, v151, v96
	s_and_saveexec_b64 s[2:3], s[36:37]
	s_cbranch_execz .LBB0_764
	v_readlane_b32 s4, v250, 32
	v_readlane_b32 s5, v250, 33
	s_add_u32 s4, s4, s24
	s_addc_u32 s5, s5, s25
	v_lshl_add_u64 v[98:99], v[138:139], 2, s[4:5]
	s_waitcnt lgkmcnt(0)
	v_add_f32_e32 v96, v96, v97
	global_store_dword v[98:99], v96, off offset:64

; __device__ __forceinline__ unsigned cvt_pk_bf16(float lo, float hi) { unsigned r; asm volatile("v_cvt_pk_bf16_f32 %0, %1, %2" : "=v"(r) : "v"(lo), "v"(hi)); return r; }
;     __device__ __forceinline__ void operator()(const f32x4 (&acc)[2][2][4][2], const Unit& u, int wr, int wc, int fr, int fq) const {
;     ...
;                         if (R32) r = *(const f32x4*)(R32 + ro + bj * HALF + n * 16);
;                         else { typedef unsigned u32x2_t __attribute__((ext_vector_type(2))); const u32x2_t rw = *(const u32x2_t*)(R16 + ro + bj * HALF + n * 16); const unsigned r0 = rw.x, r1 = rw.y;
;                             r = (f32x4){__builtin_bit_cast(float, r0 << 16), __builtin_bit_cast(float, r0 & 0xffff0000u), __builtin_bit_cast(float, r1 << 16), __builtin_bit_cast(float, r1 & 0xffff0000u)}; }
;                         const f32x4 v = acc[ai][bj][m][n] + r;
;                         typedef unsigned u32x2_s __attribute__((ext_vector_type(2))); u32x2_s w; w.x = cvt_pk_bf16(v[0], v[1]); w.y = cvt_pk_bf16(v[2], v[3]);
;                         *(u32x2_s*)(XB + ro + bj * HALF + n * 16) = w;
;                         s += (v[0] * v[0] + v[1] * v[1]) + (v[2] * v[2] + v[3] * v[3]); }
;                 s += __shfl_xor(s, 16); s += __shfl_xor(s, 32);
;                 if (fq == 0) ss2[(size_t)(u.pn * 4 + wc) * MT + row] = s; }
.LBB0_766:
	s_andn2_b64 vcc, exec, s[2:3]
	v_lshl_add_u64 v[102:103], v[106:107], 1, s[48:49]
	s_cbranch_vccnz .LBB0_768
	s_mov_b32 s100, 0x90000
	s_mov_b32 s101, 0
	v_lshl_add_u64 v[202:203], v[204:205], 0, s[100:101]
	v_lshl_add_u64 v[208:209], v[202:203], 0, v[236:237]
	global_load_dwordx4 v[164:167], v[208:209], off
	v_lshl_add_u64 v[208:209], v[208:209], 0, v[206:207]
	global_load_dwordx4 v[168:171], v[208:209], off
	s_waitcnt vmcnt(10)
	ds_write_b128 v235, v[172:175]
	ds_write_b128 v235, v[176:179] offset:1152
	s_waitcnt lgkmcnt(0)
	ds_read_b64 v[226:227], v234
	ds_read_b64 v[228:229], v234 offset:32
	ds_read_b64 v[230:231], v234 offset:64
	ds_read_b64 v[232:233], v234 offset:96
	s_waitcnt lgkmcnt(0)
	v_lshlrev_b32_e32 v96, 16, v226
	v_and_b32_e32 v97, 0xffff0000, v226
	v_lshlrev_b32_e32 v98, 16, v227
	v_and_b32_e32 v99, 0xffff0000, v227
.LBB0_768:
	v_pk_add_f32 v[98:99], v[94:95], v[98:99]
	v_pk_add_f32 v[104:105], v[92:93], v[96:97]
	v_lshl_add_u64 v[96:97], v[106:107], 1, s[90:91]
	v_cvt_pk_bf16_f32 v92, v104, v105
	v_cvt_pk_bf16_f32 v93, v98, v99
	s_and_b64 vcc, exec, s[40:41]
	s_mov_b64 s[2:3], -1
	ds_write_b64 v234, v[92:93]
	s_cbranch_vccnz .LBB0_770
	global_load_dwordx4 v[92:95], v[100:101], off offset:64
	s_waitcnt vmcnt(0)
	s_mov_b64 s[2:3], 0
.LBB0_770:
	s_andn2_b64 vcc, exec, s[2:3]
	s_cbranch_vccnz .LBB0_772
	v_lshlrev_b32_e32 v92, 16, v228
	v_and_b32_e32 v93, 0xffff0000, v228
	v_lshlrev_b32_e32 v94, 16, v229
	v_and_b32_e32 v95, 0xffff0000, v229
.LBB0_772:
	v_pk_add_f32 v[94:95], v[90:91], v[94:95]
	v_pk_add_f32 v[92:93], v[88:89], v[92:93]
	s_and_b64 vcc, exec, s[40:41]
	v_cvt_pk_bf16_f32 v88, v92, v93
	v_cvt_pk_bf16_f32 v89, v94, v95
	s_mov_b64 s[2:3], -1
	ds_write_b64 v234, v[88:89] offset:32
	s_cbranch_vccnz .LBB0_774
	global_load_dwordx4 v[88:91], v[100:101], off offset:512
	s_waitcnt vmcnt(0)
	s_mov_b64 s[2:3], 0
.LBB0_774:
	s_andn2_b64 vcc, exec, s[2:3]
	s_cbranch_vccnz .LBB0_776
	v_lshlrev_b32_e32 v88, 16, v230
	v_and_b32_e32 v89, 0xffff0000, v230
	v_lshlrev_b32_e32 v90, 16, v231
	v_and_b32_e32 v91, 0xffff0000, v231
.LBB0_776:
	v_pk_add_f32 v[90:91], v[86:87], v[90:91]
	v_pk_add_f32 v[88:89], v[84:85], v[88:89]
	s_and_b64 vcc, exec, s[40:41]
	v_cvt_pk_bf16_f32 v84, v88, v89
	v_cvt_pk_bf16_f32 v85, v90, v91
	s_mov_b64 s[2:3], -1
	ds_write_b64 v234, v[84:85] offset:64
	s_cbranch_vccnz .LBB0_778
	global_load_dwordx4 v[84:87], v[100:101], off offset:576
	s_waitcnt vmcnt(0)
	s_mov_b64 s[2:3], 0
.LBB0_778:
	s_andn2_b64 vcc, exec, s[2:3]
	s_cbranch_vccnz .LBB0_780
	v_lshlrev_b32_e32 v84, 16, v232
	v_and_b32_e32 v85, 0xffff0000, v232
	v_lshlrev_b32_e32 v86, 16, v233
	v_and_b32_e32 v87, 0xffff0000, v233
.LBB0_780:
	v_mul_f32_e32 v93, v93, v93
	v_mul_f32_e32 v100, v105, v105
	v_mul_f32_e32 v99, v99, v99
	v_fmac_f32_e32 v93, v92, v92
	v_mul_f32_e32 v92, v95, v95
	v_mul_f32_e32 v89, v89, v89
	v_fmac_f32_e32 v100, v104, v104
	v_fmac_f32_e32 v99, v98, v98
	v_fmac_f32_e32 v92, v94, v94
	v_fmac_f32_e32 v89, v88, v88
	v_mul_f32_e32 v88, v91, v91
	v_pk_add_f32 v[82:83], v[82:83], v[86:87]
	v_pk_add_f32 v[84:85], v[80:81], v[84:85]
	v_add_f32_e32 v98, v100, v99
	v_add_f32_e32 v92, v93, v92
	v_fmac_f32_e32 v88, v90, v90
	v_mul_f32_e32 v80, v85, v85
	v_mul_f32_e32 v81, v83, v83
	v_add_f32_e32 v92, v98, v92
	v_add_f32_e32 v88, v89, v88
	v_fmac_f32_e32 v80, v84, v84
	v_fmac_f32_e32 v81, v82, v82
	v_add_f32_e32 v88, v92, v88
	v_add_f32_e32 v80, v80, v81
	v_add_f32_e32 v80, v88, v80
	ds_bpermute_b32 v81, v150, v80
	v_cvt_pk_bf16_f32 v84, v84, v85
	v_cvt_pk_bf16_f32 v85, v82, v83
	ds_write_b64 v234, v[84:85] offset:96
	s_waitcnt lgkmcnt(0)
	ds_read_b128 v[226:229], v235
	ds_read_b128 v[230:233], v235 offset:1152
	v_lshl_add_u64 v[238:239], v[96:97], 0, v[236:237]
	s_waitcnt lgkmcnt(1)
	global_store_dwordx4 v[238:239], v[226:229], off
	v_lshl_add_u64 v[238:239], v[238:239], 0, v[206:207]
	s_waitcnt lgkmcnt(0)
	global_store_dwordx4 v[238:239], v[230:233], off
	s_waitcnt lgkmcnt(0)
	v_add_f32_e32 v80, v80, v81
	ds_bpermute_b32 v81, v151, v80
	s_and_saveexec_b64 s[2:3], s[36:37]
	s_cbranch_execz .LBB0_782
	v_readlane_b32 s4, v250, 32
	v_readlane_b32 s5, v250, 33
	s_add_u32 s4, s4, s24
	s_addc_u32 s5, s5, s25
	v_lshl_add_u64 v[82:83], v[138:139], 2, s[4:5]
	s_waitcnt lgkmcnt(0)
	v_add_f32_e32 v80, v80, v81
	global_store_dword v[82:83], v80, off offset:128

; __device__ __forceinline__ unsigned cvt_pk_bf16(float lo, float hi) { unsigned r; asm volatile("v_cvt_pk_bf16_f32 %0, %1, %2" : "=v"(r) : "v"(lo), "v"(hi)); return r; }
;     __device__ __forceinline__ void operator()(const f32x4 (&acc)[2][2][4][2], const Unit& u, int wr, int wc, int fr, int fq) const {
;     ...
;                         if (R32) r = *(const f32x4*)(R32 + ro + bj * HALF + n * 16);
;                         else { typedef unsigned u32x2_t __attribute__((ext_vector_type(2))); const u32x2_t rw = *(const u32x2_t*)(R16 + ro + bj * HALF + n * 16); const unsigned r0 = rw.x, r1 = rw.y;
;                             r = (f32x4){__builtin_bit_cast(float, r0 << 16), __builtin_bit_cast(float, r0 & 0xffff0000u), __builtin_bit_cast(float, r1 << 16), __builtin_bit_cast(float, r1 & 0xffff0000u)}; }
;                         const f32x4 v = acc[ai][bj][m][n] + r;
;                         typedef unsigned u32x2_s __attribute__((ext_vector_type(2))); u32x2_s w; w.x = cvt_pk_bf16(v[0], v[1]); w.y = cvt_pk_bf16(v[2], v[3]);
;                         *(u32x2_s*)(XB + ro + bj * HALF + n * 16) = w;
;                         s += (v[0] * v[0] + v[1] * v[1]) + (v[2] * v[2] + v[3] * v[3]); }
;                 s += __shfl_xor(s, 16); s += __shfl_xor(s, 32);
;                 if (fq == 0) ss2[(size_t)(u.pn * 4 + wc) * MT + row] = s; }
.LBB0_784:
	s_andn2_b64 vcc, exec, s[2:3]
	v_lshl_add_u64 v[86:87], v[90:91], 1, s[48:49]
	s_cbranch_vccnz .LBB0_786
	s_mov_b32 s100, 0xa0000
	s_mov_b32 s101, 0
	v_lshl_add_u64 v[202:203], v[204:205], 0, s[100:101]
	v_lshl_add_u64 v[208:209], v[202:203], 0, v[236:237]
	global_load_dwordx4 v[172:175], v[208:209], off
	v_lshl_add_u64 v[208:209], v[208:209], 0, v[206:207]
	global_load_dwordx4 v[176:179], v[208:209], off
	s_waitcnt vmcnt(12)
	ds_write_b128 v235, v[194:197]
	ds_write_b128 v235, v[198:201] offset:1152
	s_waitcnt lgkmcnt(0)
	ds_read_b64 v[226:227], v234
	ds_read_b64 v[228:229], v234 offset:32
	ds_read_b64 v[230:231], v234 offset:64
	ds_read_b64 v[232:233], v234 offset:96
	s_waitcnt lgkmcnt(0)
	v_lshlrev_b32_e32 v80, 16, v226
	v_and_b32_e32 v81, 0xffff0000, v226
	v_lshlrev_b32_e32 v82, 16, v227
	v_and_b32_e32 v83, 0xffff0000, v227
.LBB0_786:
	v_pk_add_f32 v[82:83], v[78:79], v[82:83]
	v_pk_add_f32 v[88:89], v[76:77], v[80:81]
	v_lshl_add_u64 v[80:81], v[90:91], 1, s[90:91]
	v_cvt_pk_bf16_f32 v76, v88, v89
	v_cvt_pk_bf16_f32 v77, v82, v83
	s_and_b64 vcc, exec, s[40:41]
	s_mov_b64 s[2:3], -1
	ds_write_b64 v234, v[76:77]
	s_cbranch_vccnz .LBB0_788
	global_load_dwordx4 v[76:79], v[84:85], off offset:64
	s_waitcnt vmcnt(0)
	s_mov_b64 s[2:3], 0
.LBB0_788:
	s_andn2_b64 vcc, exec, s[2:3]
	s_cbranch_vccnz .LBB0_790
	v_lshlrev_b32_e32 v76, 16, v228
	v_and_b32_e32 v77, 0xffff0000, v228
	v_lshlrev_b32_e32 v78, 16, v229
	v_and_b32_e32 v79, 0xffff0000, v229
.LBB0_790:
	v_pk_add_f32 v[78:79], v[74:75], v[78:79]
	v_pk_add_f32 v[76:77], v[72:73], v[76:77]
	s_and_b64 vcc, exec, s[40:41]
	v_cvt_pk_bf16_f32 v72, v76, v77
	v_cvt_pk_bf16_f32 v73, v78, v79
	s_mov_b64 s[2:3], -1
	ds_write_b64 v234, v[72:73] offset:32
	s_cbranch_vccnz .LBB0_792
	global_load_dwordx4 v[72:75], v[84:85], off offset:512
	s_waitcnt vmcnt(0)
	s_mov_b64 s[2:3], 0
.LBB0_792:
	s_andn2_b64 vcc, exec, s[2:3]
	s_cbranch_vccnz .LBB0_794
	v_lshlrev_b32_e32 v72, 16, v230
	v_and_b32_e32 v73, 0xffff0000, v230
	v_lshlrev_b32_e32 v74, 16, v231
	v_and_b32_e32 v75, 0xffff0000, v231
.LBB0_794:
	v_pk_add_f32 v[74:75], v[70:71], v[74:75]
	v_pk_add_f32 v[72:73], v[68:69], v[72:73]
	s_and_b64 vcc, exec, s[40:41]
	v_cvt_pk_bf16_f32 v68, v72, v73
	v_cvt_pk_bf16_f32 v69, v74, v75
	s_mov_b64 s[2:3], -1
	ds_write_b64 v234, v[68:69] offset:64
	s_cbranch_vccnz .LBB0_796
	global_load_dwordx4 v[68:71], v[84:85], off offset:576
	s_waitcnt vmcnt(0)
	s_mov_b64 s[2:3], 0
.LBB0_796:
	s_andn2_b64 vcc, exec, s[2:3]
	s_cbranch_vccnz .LBB0_798
	v_lshlrev_b32_e32 v68, 16, v232
	v_and_b32_e32 v69, 0xffff0000, v232
	v_lshlrev_b32_e32 v70, 16, v233
	v_and_b32_e32 v71, 0xffff0000, v233
.LBB0_798:
	v_mul_f32_e32 v77, v77, v77
	v_mul_f32_e32 v84, v89, v89
	v_mul_f32_e32 v83, v83, v83
	v_fmac_f32_e32 v77, v76, v76
	v_mul_f32_e32 v76, v79, v79
	v_mul_f32_e32 v73, v73, v73
	v_fmac_f32_e32 v84, v88, v88
	v_fmac_f32_e32 v83, v82, v82
	v_fmac_f32_e32 v76, v78, v78
	v_fmac_f32_e32 v73, v72, v72
	v_mul_f32_e32 v72, v75, v75
	v_pk_add_f32 v[66:67], v[66:67], v[70:71]
	v_pk_add_f32 v[68:69], v[64:65], v[68:69]
	v_add_f32_e32 v82, v84, v83
	v_add_f32_e32 v76, v77, v76
	v_fmac_f32_e32 v72, v74, v74
	v_mul_f32_e32 v64, v69, v69
	v_mul_f32_e32 v65, v67, v67
	v_add_f32_e32 v76, v82, v76
	v_add_f32_e32 v72, v73, v72
	v_fmac_f32_e32 v64, v68, v68
	v_fmac_f32_e32 v65, v66, v66
	v_add_f32_e32 v72, v76, v72
	v_add_f32_e32 v64, v64, v65
	v_add_f32_e32 v64, v72, v64
	ds_bpermute_b32 v65, v150, v64
	v_cvt_pk_bf16_f32 v68, v68, v69
	v_cvt_pk_bf16_f32 v69, v66, v67
	ds_write_b64 v234, v[68:69] offset:96
	s_waitcnt lgkmcnt(0)
	ds_read_b128 v[226:229], v235
	ds_read_b128 v[230:233], v235 offset:1152
	v_lshl_add_u64 v[238:239], v[80:81], 0, v[236:237]
	s_waitcnt lgkmcnt(1)
	global_store_dwordx4 v[238:239], v[226:229], off
	v_lshl_add_u64 v[238:239], v[238:239], 0, v[206:207]
	s_waitcnt lgkmcnt(0)
	global_store_dwordx4 v[238:239], v[230:233], off
	s_waitcnt lgkmcnt(0)
	v_add_f32_e32 v64, v64, v65
	ds_bpermute_b32 v65, v151, v64
	s_and_saveexec_b64 s[2:3], s[36:37]
	s_cbranch_execz .LBB0_800
	v_readlane_b32 s4, v250, 32
	v_readlane_b32 s5, v250, 33
	s_add_u32 s4, s4, s24
	s_addc_u32 s5, s5, s25
	v_lshl_add_u64 v[66:67], v[138:139], 2, s[4:5]
	s_waitcnt lgkmcnt(0)
	v_add_f32_e32 v64, v64, v65
	global_store_dword v[66:67], v64, off offset:192

; __device__ __forceinline__ unsigned cvt_pk_bf16(float lo, float hi) { unsigned r; asm volatile("v_cvt_pk_bf16_f32 %0, %1, %2" : "=v"(r) : "v"(lo), "v"(hi)); return r; }
;     __device__ __forceinline__ void operator()(const f32x4 (&acc)[2][2][4][2], const Unit& u, int wr, int wc, int fr, int fq) const {
;     ...
;                         if (R32) r = *(const f32x4*)(R32 + ro + bj * HALF + n * 16);
;                         else { typedef unsigned u32x2_t __attribute__((ext_vector_type(2))); const u32x2_t rw = *(const u32x2_t*)(R16 + ro + bj * HALF + n * 16); const unsigned r0 = rw.x, r1 = rw.y;
;                             r = (f32x4){__builtin_bit_cast(float, r0 << 16), __builtin_bit_cast(float, r0 & 0xffff0000u), __builtin_bit_cast(float, r1 << 16), __builtin_bit_cast(float, r1 & 0xffff0000u)}; }
;                         const f32x4 v = acc[ai][bj][m][n] + r;
;                         typedef unsigned u32x2_s __attribute__((ext_vector_type(2))); u32x2_s w; w.x = cvt_pk_bf16(v[0], v[1]); w.y = cvt_pk_bf16(v[2], v[3]);
;                         *(u32x2_s*)(XB + ro + bj * HALF + n * 16) = w;
;                         s += (v[0] * v[0] + v[1] * v[1]) + (v[2] * v[2] + v[3] * v[3]); }
;                 s += __shfl_xor(s, 16); s += __shfl_xor(s, 32);
;                 if (fq == 0) ss2[(size_t)(u.pn * 4 + wc) * MT + row] = s; }
.LBB0_802:
	s_andn2_b64 vcc, exec, s[2:3]
	v_lshl_add_u64 v[70:71], v[74:75], 1, s[48:49]
	s_cbranch_vccnz .LBB0_804
	s_mov_b32 s100, 0xb0000
	s_mov_b32 s101, 0
	v_lshl_add_u64 v[202:203], v[204:205], 0, s[100:101]
	v_lshl_add_u64 v[208:209], v[202:203], 0, v[236:237]
	global_load_dwordx4 v[194:197], v[208:209], off
	v_lshl_add_u64 v[208:209], v[208:209], 0, v[206:207]
	global_load_dwordx4 v[198:201], v[208:209], off
	s_waitcnt vmcnt(12)
	ds_write_b128 v235, v[156:159]
	ds_write_b128 v235, v[160:163] offset:1152
	s_waitcnt lgkmcnt(0)
	ds_read_b64 v[226:227], v234
	ds_read_b64 v[228:229], v234 offset:32
	ds_read_b64 v[230:231], v234 offset:64
	ds_read_b64 v[232:233], v234 offset:96
	s_waitcnt lgkmcnt(0)
	v_lshlrev_b32_e32 v64, 16, v226
	s_waitcnt lgkmcnt(0)
	v_and_b32_e32 v65, 0xffff0000, v226
	v_lshlrev_b32_e32 v66, 16, v227
	v_and_b32_e32 v67, 0xffff0000, v227
.LBB0_804:
	v_pk_add_f32 v[66:67], v[62:63], v[66:67]
	s_waitcnt lgkmcnt(0)
	v_pk_add_f32 v[72:73], v[60:61], v[64:65]
	v_lshl_add_u64 v[64:65], v[74:75], 1, s[90:91]
	v_cvt_pk_bf16_f32 v60, v72, v73
	v_cvt_pk_bf16_f32 v61, v66, v67
	s_and_b64 vcc, exec, s[40:41]
	s_mov_b64 s[2:3], -1
	ds_write_b64 v234, v[60:61]
	s_cbranch_vccnz .LBB0_806
	global_load_dwordx4 v[60:63], v[68:69], off offset:64
	s_waitcnt vmcnt(0)
	s_mov_b64 s[2:3], 0
.LBB0_806:
	s_andn2_b64 vcc, exec, s[2:3]
	s_cbranch_vccnz .LBB0_808
	v_lshlrev_b32_e32 v60, 16, v228
	v_and_b32_e32 v61, 0xffff0000, v228
	v_lshlrev_b32_e32 v62, 16, v229
	v_and_b32_e32 v63, 0xffff0000, v229
.LBB0_808:
	v_pk_add_f32 v[62:63], v[58:59], v[62:63]
	v_pk_add_f32 v[60:61], v[56:57], v[60:61]
	s_and_b64 vcc, exec, s[40:41]
	v_cvt_pk_bf16_f32 v56, v60, v61
	v_cvt_pk_bf16_f32 v57, v62, v63
	s_mov_b64 s[2:3], -1
	ds_write_b64 v234, v[56:57] offset:32
	s_cbranch_vccnz .LBB0_810
	global_load_dwordx4 v[56:59], v[68:69], off offset:512
	s_waitcnt vmcnt(0)
	s_mov_b64 s[2:3], 0
.LBB0_810:
	s_andn2_b64 vcc, exec, s[2:3]
	s_cbranch_vccnz .LBB0_812
	v_lshlrev_b32_e32 v56, 16, v230
	v_and_b32_e32 v57, 0xffff0000, v230
	v_lshlrev_b32_e32 v58, 16, v231
	v_and_b32_e32 v59, 0xffff0000, v231
.LBB0_812:
	v_pk_add_f32 v[58:59], v[54:55], v[58:59]
	v_pk_add_f32 v[56:57], v[52:53], v[56:57]
	s_and_b64 vcc, exec, s[40:41]
	v_cvt_pk_bf16_f32 v52, v56, v57
	v_cvt_pk_bf16_f32 v53, v58, v59
	s_mov_b64 s[2:3], -1
	ds_write_b64 v234, v[52:53] offset:64
	s_cbranch_vccnz .LBB0_814
	global_load_dwordx4 v[52:55], v[68:69], off offset:576
	s_waitcnt vmcnt(0)
	s_mov_b64 s[2:3], 0
.LBB0_814:
	s_andn2_b64 vcc, exec, s[2:3]
	s_cbranch_vccnz .LBB0_816
	v_lshlrev_b32_e32 v52, 16, v232
	v_and_b32_e32 v53, 0xffff0000, v232
	v_lshlrev_b32_e32 v54, 16, v233
	v_and_b32_e32 v55, 0xffff0000, v233
.LBB0_816:
	v_mul_f32_e32 v61, v61, v61
	v_mul_f32_e32 v68, v73, v73
	v_mul_f32_e32 v67, v67, v67
	v_fmac_f32_e32 v61, v60, v60
	v_mul_f32_e32 v60, v63, v63
	v_mul_f32_e32 v57, v57, v57
	v_fmac_f32_e32 v68, v72, v72
	v_fmac_f32_e32 v67, v66, v66
	v_fmac_f32_e32 v60, v62, v62
	v_fmac_f32_e32 v57, v56, v56
	v_mul_f32_e32 v56, v59, v59
	v_pk_add_f32 v[50:51], v[50:51], v[54:55]
	v_pk_add_f32 v[52:53], v[48:49], v[52:53]
	v_add_f32_e32 v66, v68, v67
	v_add_f32_e32 v60, v61, v60
	v_fmac_f32_e32 v56, v58, v58
	v_mul_f32_e32 v48, v53, v53
	v_mul_f32_e32 v49, v51, v51
	v_add_f32_e32 v60, v66, v60
	v_add_f32_e32 v56, v57, v56
	v_fmac_f32_e32 v48, v52, v52
	v_fmac_f32_e32 v49, v50, v50
	v_add_f32_e32 v56, v60, v56
	v_add_f32_e32 v48, v48, v49
	v_add_f32_e32 v48, v56, v48
	ds_bpermute_b32 v49, v150, v48
	v_cvt_pk_bf16_f32 v52, v52, v53
	v_cvt_pk_bf16_f32 v53, v50, v51
	ds_write_b64 v234, v[52:53] offset:96
	s_waitcnt lgkmcnt(0)
	ds_read_b128 v[226:229], v235
	ds_read_b128 v[230:233], v235 offset:1152
	v_lshl_add_u64 v[238:239], v[64:65], 0, v[236:237]
	s_waitcnt lgkmcnt(1)
	global_store_dwordx4 v[238:239], v[226:229], off
	v_lshl_add_u64 v[238:239], v[238:239], 0, v[206:207]
	s_waitcnt lgkmcnt(0)
	global_store_dwordx4 v[238:239], v[230:233], off
	s_waitcnt lgkmcnt(0)
	v_add_f32_e32 v48, v48, v49
	ds_bpermute_b32 v49, v151, v48
	s_and_saveexec_b64 s[2:3], s[36:37]
	s_cbranch_execz .LBB0_818
	v_readlane_b32 s4, v250, 32
	v_readlane_b32 s5, v250, 33
	s_add_u32 s4, s4, s24
	s_addc_u32 s5, s5, s25
	v_lshl_add_u64 v[50:51], v[138:139], 2, s[4:5]
	s_waitcnt lgkmcnt(0)
	v_add_f32_e32 v48, v48, v49
	global_store_dword v[50:51], v48, off offset:512

; __device__ __forceinline__ unsigned cvt_pk_bf16(float lo, float hi) { unsigned r; asm volatile("v_cvt_pk_bf16_f32 %0, %1, %2" : "=v"(r) : "v"(lo), "v"(hi)); return r; }
;     __device__ __forceinline__ void operator()(const f32x4 (&acc)[2][2][4][2], const Unit& u, int wr, int wc, int fr, int fq) const {
;     ...
;                         if (R32) r = *(const f32x4*)(R32 + ro + bj * HALF + n * 16);
;                         else { typedef unsigned u32x2_t __attribute__((ext_vector_type(2))); const u32x2_t rw = *(const u32x2_t*)(R16 + ro + bj * HALF + n * 16); const unsigned r0 = rw.x, r1 = rw.y;
;                             r = (f32x4){__builtin_bit_cast(float, r0 << 16), __builtin_bit_cast(float, r0 & 0xffff0000u), __builtin_bit_cast(float, r1 << 16), __builtin_bit_cast(float, r1 & 0xffff0000u)}; }
;                         const f32x4 v = acc[ai][bj][m][n] + r;
;                         typedef unsigned u32x2_s __attribute__((ext_vector_type(2))); u32x2_s w; w.x = cvt_pk_bf16(v[0], v[1]); w.y = cvt_pk_bf16(v[2], v[3]);
;                         *(u32x2_s*)(XB + ro + bj * HALF + n * 16) = w;
;                         s += (v[0] * v[0] + v[1] * v[1]) + (v[2] * v[2] + v[3] * v[3]); }
;                 s += __shfl_xor(s, 16); s += __shfl_xor(s, 32);
;                 if (fq == 0) ss2[(size_t)(u.pn * 4 + wc) * MT + row] = s; }
.LBB0_820:
	s_andn2_b64 vcc, exec, s[2:3]
	v_lshl_add_u64 v[54:55], v[58:59], 1, s[48:49]
	s_cbranch_vccnz .LBB0_822
	s_waitcnt vmcnt(10)
	ds_write_b128 v235, v[164:167]
	ds_write_b128 v235, v[168:171] offset:1152
	s_waitcnt lgkmcnt(0)
	ds_read_b64 v[226:227], v234
	ds_read_b64 v[228:229], v234 offset:32
	ds_read_b64 v[230:231], v234 offset:64
	ds_read_b64 v[232:233], v234 offset:96
	s_waitcnt lgkmcnt(0)
	v_lshlrev_b32_e32 v48, 16, v226
	s_waitcnt lgkmcnt(0)
	v_and_b32_e32 v49, 0xffff0000, v226
	v_lshlrev_b32_e32 v50, 16, v227
	v_and_b32_e32 v51, 0xffff0000, v227
.LBB0_822:
	v_pk_add_f32 v[50:51], v[46:47], v[50:51]
	s_waitcnt lgkmcnt(0)
	v_pk_add_f32 v[56:57], v[44:45], v[48:49]
	v_lshl_add_u64 v[48:49], v[58:59], 1, s[90:91]
	v_cvt_pk_bf16_f32 v44, v56, v57
	v_cvt_pk_bf16_f32 v45, v50, v51
	s_and_b64 vcc, exec, s[40:41]
	s_mov_b64 s[2:3], -1
	ds_write_b64 v234, v[44:45]
	s_cbranch_vccnz .LBB0_824
	global_load_dwordx4 v[44:47], v[52:53], off offset:64
	s_waitcnt vmcnt(0)
	s_mov_b64 s[2:3], 0
.LBB0_824:
	s_andn2_b64 vcc, exec, s[2:3]
	s_cbranch_vccnz .LBB0_826
	v_lshlrev_b32_e32 v44, 16, v228
	v_and_b32_e32 v45, 0xffff0000, v228
	v_lshlrev_b32_e32 v46, 16, v229
	v_and_b32_e32 v47, 0xffff0000, v229
.LBB0_826:
	v_pk_add_f32 v[46:47], v[42:43], v[46:47]
	v_pk_add_f32 v[44:45], v[40:41], v[44:45]
	s_and_b64 vcc, exec, s[40:41]
	v_cvt_pk_bf16_f32 v40, v44, v45
	v_cvt_pk_bf16_f32 v41, v46, v47
	s_mov_b64 s[2:3], -1
	ds_write_b64 v234, v[40:41] offset:32
	s_cbranch_vccnz .LBB0_828
	global_load_dwordx4 v[40:43], v[52:53], off offset:512
	s_waitcnt vmcnt(0)
	s_mov_b64 s[2:3], 0
.LBB0_828:
	s_andn2_b64 vcc, exec, s[2:3]
	s_cbranch_vccnz .LBB0_830
	v_lshlrev_b32_e32 v40, 16, v230
	v_and_b32_e32 v41, 0xffff0000, v230
	v_lshlrev_b32_e32 v42, 16, v231
	v_and_b32_e32 v43, 0xffff0000, v231
.LBB0_830:
	v_pk_add_f32 v[42:43], v[38:39], v[42:43]
	v_pk_add_f32 v[40:41], v[36:37], v[40:41]
	s_and_b64 vcc, exec, s[40:41]
	v_cvt_pk_bf16_f32 v36, v40, v41
	v_cvt_pk_bf16_f32 v37, v42, v43
	s_mov_b64 s[2:3], -1
	ds_write_b64 v234, v[36:37] offset:64
	s_cbranch_vccnz .LBB0_832
	global_load_dwordx4 v[36:39], v[52:53], off offset:576
	s_waitcnt vmcnt(0)
	s_mov_b64 s[2:3], 0
.LBB0_832:
	s_andn2_b64 vcc, exec, s[2:3]
	s_cbranch_vccnz .LBB0_834
	v_lshlrev_b32_e32 v36, 16, v232
	v_and_b32_e32 v37, 0xffff0000, v232
	v_lshlrev_b32_e32 v38, 16, v233
	v_and_b32_e32 v39, 0xffff0000, v233
.LBB0_834:
	v_mul_f32_e32 v45, v45, v45
	v_mul_f32_e32 v52, v57, v57
	v_mul_f32_e32 v51, v51, v51
	v_fmac_f32_e32 v45, v44, v44
	v_mul_f32_e32 v44, v47, v47
	v_mul_f32_e32 v41, v41, v41
	v_fmac_f32_e32 v52, v56, v56
	v_fmac_f32_e32 v51, v50, v50
	v_fmac_f32_e32 v44, v46, v46
	v_fmac_f32_e32 v41, v40, v40
	v_mul_f32_e32 v40, v43, v43
	v_pk_add_f32 v[34:35], v[34:35], v[38:39]
	v_pk_add_f32 v[36:37], v[32:33], v[36:37]
	v_add_f32_e32 v50, v52, v51
	v_add_f32_e32 v44, v45, v44
	v_fmac_f32_e32 v40, v42, v42
	v_mul_f32_e32 v32, v37, v37
	v_mul_f32_e32 v33, v35, v35
	v_add_f32_e32 v44, v50, v44
	v_add_f32_e32 v40, v41, v40
	v_fmac_f32_e32 v32, v36, v36
	v_fmac_f32_e32 v33, v34, v34
	v_add_f32_e32 v40, v44, v40
	v_add_f32_e32 v32, v32, v33
	v_add_f32_e32 v32, v40, v32
	ds_bpermute_b32 v33, v150, v32
	v_cvt_pk_bf16_f32 v36, v36, v37
	v_cvt_pk_bf16_f32 v37, v34, v35
	ds_write_b64 v234, v[36:37] offset:96
	s_waitcnt lgkmcnt(0)
	ds_read_b128 v[226:229], v235
	ds_read_b128 v[230:233], v235 offset:1152
	v_lshl_add_u64 v[238:239], v[48:49], 0, v[236:237]
	s_waitcnt lgkmcnt(1)
	global_store_dwordx4 v[238:239], v[226:229], off
	v_lshl_add_u64 v[238:239], v[238:239], 0, v[206:207]
	s_waitcnt lgkmcnt(0)
	global_store_dwordx4 v[238:239], v[230:233], off
	s_waitcnt lgkmcnt(0)
	v_add_f32_e32 v32, v32, v33
	ds_bpermute_b32 v33, v151, v32
	s_and_saveexec_b64 s[2:3], s[36:37]
	s_cbranch_execz .LBB0_836
	v_readlane_b32 s4, v250, 32
	v_readlane_b32 s5, v250, 33
	s_add_u32 s4, s4, s24
	s_addc_u32 s5, s5, s25
	v_lshl_add_u64 v[34:35], v[138:139], 2, s[4:5]
	s_waitcnt lgkmcnt(0)
	v_add_f32_e32 v32, v32, v33
	global_store_dword v[34:35], v32, off offset:576

; __device__ __forceinline__ unsigned cvt_pk_bf16(float lo, float hi) { unsigned r; asm volatile("v_cvt_pk_bf16_f32 %0, %1, %2" : "=v"(r) : "v"(lo), "v"(hi)); return r; }
;     __device__ __forceinline__ void operator()(const f32x4 (&acc)[2][2][4][2], const Unit& u, int wr, int wc, int fr, int fq) const {
;     ...
;                         if (R32) r = *(const f32x4*)(R32 + ro + bj * HALF + n * 16);
;                         else { typedef unsigned u32x2_t __attribute__((ext_vector_type(2))); const u32x2_t rw = *(const u32x2_t*)(R16 + ro + bj * HALF + n * 16); const unsigned r0 = rw.x, r1 = rw.y;
;                             r = (f32x4){__builtin_bit_cast(float, r0 << 16), __builtin_bit_cast(float, r0 & 0xffff0000u), __builtin_bit_cast(float, r1 << 16), __builtin_bit_cast(float, r1 & 0xffff0000u)}; }
;                         const f32x4 v = acc[ai][bj][m][n] + r;
;                         typedef unsigned u32x2_s __attribute__((ext_vector_type(2))); u32x2_s w; w.x = cvt_pk_bf16(v[0], v[1]); w.y = cvt_pk_bf16(v[2], v[3]);
;                         *(u32x2_s*)(XB + ro + bj * HALF + n * 16) = w;
;                         s += (v[0] * v[0] + v[1] * v[1]) + (v[2] * v[2] + v[3] * v[3]); }
;                 s += __shfl_xor(s, 16); s += __shfl_xor(s, 32);
;                 if (fq == 0) ss2[(size_t)(u.pn * 4 + wc) * MT + row] = s; }
.LBB0_838:
	s_andn2_b64 vcc, exec, s[2:3]
	v_lshl_add_u64 v[38:39], v[42:43], 1, s[48:49]
	s_cbranch_vccnz .LBB0_840
	s_waitcnt vmcnt(8)
	ds_write_b128 v235, v[172:175]
	ds_write_b128 v235, v[176:179] offset:1152
	s_waitcnt lgkmcnt(0)
	ds_read_b64 v[226:227], v234
	ds_read_b64 v[228:229], v234 offset:32
	ds_read_b64 v[230:231], v234 offset:64
	ds_read_b64 v[232:233], v234 offset:96
	s_waitcnt lgkmcnt(0)
	v_lshlrev_b32_e32 v32, 16, v226
	s_waitcnt lgkmcnt(0)
	v_and_b32_e32 v33, 0xffff0000, v226
	v_lshlrev_b32_e32 v34, 16, v227
	v_and_b32_e32 v35, 0xffff0000, v227
.LBB0_840:
	v_pk_add_f32 v[34:35], v[30:31], v[34:35]
	s_waitcnt lgkmcnt(0)
	v_pk_add_f32 v[40:41], v[28:29], v[32:33]
	v_lshl_add_u64 v[32:33], v[42:43], 1, s[90:91]
	v_cvt_pk_bf16_f32 v28, v40, v41
	v_cvt_pk_bf16_f32 v29, v34, v35
	s_and_b64 vcc, exec, s[40:41]
	s_mov_b64 s[2:3], -1
	ds_write_b64 v234, v[28:29]
	s_cbranch_vccnz .LBB0_842
	global_load_dwordx4 v[28:31], v[36:37], off offset:64
	s_waitcnt vmcnt(0)
	s_mov_b64 s[2:3], 0
.LBB0_842:
	s_andn2_b64 vcc, exec, s[2:3]
	s_cbranch_vccnz .LBB0_844
	v_lshlrev_b32_e32 v28, 16, v228
	v_and_b32_e32 v29, 0xffff0000, v228
	v_lshlrev_b32_e32 v30, 16, v229
	v_and_b32_e32 v31, 0xffff0000, v229
.LBB0_844:
	v_pk_add_f32 v[30:31], v[26:27], v[30:31]
	v_pk_add_f32 v[28:29], v[24:25], v[28:29]
	s_and_b64 vcc, exec, s[40:41]
	v_cvt_pk_bf16_f32 v24, v28, v29
	v_cvt_pk_bf16_f32 v25, v30, v31
	s_mov_b64 s[2:3], -1
	ds_write_b64 v234, v[24:25] offset:32
	s_cbranch_vccnz .LBB0_846
	global_load_dwordx4 v[24:27], v[36:37], off offset:512
	s_waitcnt vmcnt(0)
	s_mov_b64 s[2:3], 0
.LBB0_846:
	s_andn2_b64 vcc, exec, s[2:3]
	s_cbranch_vccnz .LBB0_848
	v_lshlrev_b32_e32 v24, 16, v230
	v_and_b32_e32 v25, 0xffff0000, v230
	v_lshlrev_b32_e32 v26, 16, v231
	v_and_b32_e32 v27, 0xffff0000, v231
.LBB0_848:
	v_pk_add_f32 v[26:27], v[22:23], v[26:27]
	v_pk_add_f32 v[24:25], v[20:21], v[24:25]
	s_and_b64 vcc, exec, s[40:41]
	v_cvt_pk_bf16_f32 v20, v24, v25
	v_cvt_pk_bf16_f32 v21, v26, v27
	s_mov_b64 s[2:3], -1
	ds_write_b64 v234, v[20:21] offset:64
	s_cbranch_vccnz .LBB0_850
	global_load_dwordx4 v[20:23], v[36:37], off offset:576
	s_waitcnt vmcnt(0)
	s_mov_b64 s[2:3], 0
.LBB0_850:
	s_andn2_b64 vcc, exec, s[2:3]
	s_cbranch_vccnz .LBB0_852
	v_lshlrev_b32_e32 v20, 16, v232
	v_and_b32_e32 v21, 0xffff0000, v232
	v_lshlrev_b32_e32 v22, 16, v233
	v_and_b32_e32 v23, 0xffff0000, v233
.LBB0_852:
	v_mul_f32_e32 v29, v29, v29
	v_mul_f32_e32 v36, v41, v41
	v_mul_f32_e32 v35, v35, v35
	v_fmac_f32_e32 v29, v28, v28
	v_mul_f32_e32 v28, v31, v31
	v_mul_f32_e32 v25, v25, v25
	v_fmac_f32_e32 v36, v40, v40
	v_fmac_f32_e32 v35, v34, v34
	v_fmac_f32_e32 v28, v30, v30
	v_fmac_f32_e32 v25, v24, v24
	v_mul_f32_e32 v24, v27, v27
	v_pk_add_f32 v[18:19], v[18:19], v[22:23]
	v_pk_add_f32 v[20:21], v[16:17], v[20:21]
	v_add_f32_e32 v34, v36, v35
	v_add_f32_e32 v28, v29, v28
	v_fmac_f32_e32 v24, v26, v26
	v_mul_f32_e32 v16, v21, v21
	v_mul_f32_e32 v17, v19, v19
	v_add_f32_e32 v28, v34, v28
	v_add_f32_e32 v24, v25, v24
	v_fmac_f32_e32 v16, v20, v20
	v_fmac_f32_e32 v17, v18, v18
	v_add_f32_e32 v24, v28, v24
	v_add_f32_e32 v16, v16, v17
	v_add_f32_e32 v16, v24, v16
	ds_bpermute_b32 v17, v150, v16
	v_cvt_pk_bf16_f32 v20, v20, v21
	v_cvt_pk_bf16_f32 v21, v18, v19
	ds_write_b64 v234, v[20:21] offset:96
	s_waitcnt lgkmcnt(0)
	ds_read_b128 v[226:229], v235
	ds_read_b128 v[230:233], v235 offset:1152
	v_lshl_add_u64 v[238:239], v[32:33], 0, v[236:237]
	s_waitcnt lgkmcnt(1)
	global_store_dwordx4 v[238:239], v[226:229], off
	v_lshl_add_u64 v[238:239], v[238:239], 0, v[206:207]
	s_waitcnt lgkmcnt(0)
	global_store_dwordx4 v[238:239], v[230:233], off
	s_waitcnt lgkmcnt(0)
	v_add_f32_e32 v16, v16, v17
	ds_bpermute_b32 v17, v151, v16
	s_and_saveexec_b64 s[2:3], s[36:37]
	s_cbranch_execz .LBB0_854
	v_readlane_b32 s4, v250, 32
	v_readlane_b32 s5, v250, 33
	s_add_u32 s4, s4, s24
	s_addc_u32 s5, s5, s25
	v_lshl_add_u64 v[18:19], v[138:139], 2, s[4:5]
	s_waitcnt lgkmcnt(0)
	v_add_f32_e32 v16, v16, v17
	global_store_dword v[18:19], v16, off offset:640

; __device__ __forceinline__ unsigned cvt_pk_bf16(float lo, float hi) { unsigned r; asm volatile("v_cvt_pk_bf16_f32 %0, %1, %2" : "=v"(r) : "v"(lo), "v"(hi)); return r; }
;     __device__ __forceinline__ void operator()(const f32x4 (&acc)[2][2][4][2], const Unit& u, int wr, int wc, int fr, int fq) const {
;     ...
;                         if (R32) r = *(const f32x4*)(R32 + ro + bj * HALF + n * 16);
;                         else { typedef unsigned u32x2_t __attribute__((ext_vector_type(2))); const u32x2_t rw = *(const u32x2_t*)(R16 + ro + bj * HALF + n * 16); const unsigned r0 = rw.x, r1 = rw.y;
;                             r = (f32x4){__builtin_bit_cast(float, r0 << 16), __builtin_bit_cast(float, r0 & 0xffff0000u), __builtin_bit_cast(float, r1 << 16), __builtin_bit_cast(float, r1 & 0xffff0000u)}; }
;                         const f32x4 v = acc[ai][bj][m][n] + r;
;                         typedef unsigned u32x2_s __attribute__((ext_vector_type(2))); u32x2_s w; w.x = cvt_pk_bf16(v[0], v[1]); w.y = cvt_pk_bf16(v[2], v[3]);
;                         *(u32x2_s*)(XB + ro + bj * HALF + n * 16) = w;
;                         s += (v[0] * v[0] + v[1] * v[1]) + (v[2] * v[2] + v[3] * v[3]); }
;                 s += __shfl_xor(s, 16); s += __shfl_xor(s, 32);
;                 if (fq == 0) ss2[(size_t)(u.pn * 4 + wc) * MT + row] = s; }
.LBB0_856:
	s_andn2_b64 vcc, exec, s[2:3]
	v_lshl_add_u64 v[20:21], v[26:27], 1, s[48:49]
	s_cbranch_vccnz .LBB0_858
	s_waitcnt vmcnt(6)
	ds_write_b128 v235, v[194:197]
	ds_write_b128 v235, v[198:201] offset:1152
	s_waitcnt lgkmcnt(0)
	ds_read_b64 v[226:227], v234
	ds_read_b64 v[228:229], v234 offset:32
	ds_read_b64 v[230:231], v234 offset:64
	ds_read_b64 v[232:233], v234 offset:96
	s_waitcnt lgkmcnt(0)
	v_lshlrev_b32_e32 v16, 16, v226
	s_waitcnt lgkmcnt(0)
	v_and_b32_e32 v17, 0xffff0000, v226
	v_lshlrev_b32_e32 v18, 16, v227
	v_and_b32_e32 v19, 0xffff0000, v227
.LBB0_858:
	v_pk_add_f32 v[18:19], v[14:15], v[18:19]
	s_waitcnt lgkmcnt(0)
	v_pk_add_f32 v[24:25], v[12:13], v[16:17]
	v_lshl_add_u64 v[16:17], v[26:27], 1, s[90:91]
	v_cvt_pk_bf16_f32 v12, v24, v25
	v_cvt_pk_bf16_f32 v13, v18, v19
	s_and_b64 vcc, exec, s[40:41]
	s_mov_b64 s[2:3], -1
	ds_write_b64 v234, v[12:13]
	s_cbranch_vccnz .LBB0_860
	global_load_dwordx4 v[12:15], v[22:23], off offset:64
	s_waitcnt vmcnt(0)
	s_mov_b64 s[2:3], 0
.LBB0_860:
	s_andn2_b64 vcc, exec, s[2:3]
	s_cbranch_vccnz .LBB0_862
	v_lshlrev_b32_e32 v12, 16, v228
	v_and_b32_e32 v13, 0xffff0000, v228
	v_lshlrev_b32_e32 v14, 16, v229
	v_and_b32_e32 v15, 0xffff0000, v229
.LBB0_862:
	v_pk_add_f32 v[14:15], v[10:11], v[14:15]
	v_pk_add_f32 v[12:13], v[8:9], v[12:13]
	s_and_b64 vcc, exec, s[40:41]
	v_cvt_pk_bf16_f32 v8, v12, v13
	v_cvt_pk_bf16_f32 v9, v14, v15
	s_mov_b64 s[2:3], -1
	ds_write_b64 v234, v[8:9] offset:32
	s_cbranch_vccnz .LBB0_864
	global_load_dwordx4 v[8:11], v[22:23], off offset:512
	s_waitcnt vmcnt(0)
	s_mov_b64 s[2:3], 0
.LBB0_864:
	s_andn2_b64 vcc, exec, s[2:3]
	s_cbranch_vccnz .LBB0_866
	v_lshlrev_b32_e32 v8, 16, v230
	v_and_b32_e32 v9, 0xffff0000, v230
	v_lshlrev_b32_e32 v10, 16, v231
	v_and_b32_e32 v11, 0xffff0000, v231
.LBB0_866:
	v_pk_add_f32 v[10:11], v[6:7], v[10:11]
	v_pk_add_f32 v[8:9], v[4:5], v[8:9]
	s_and_b64 vcc, exec, s[40:41]
	v_cvt_pk_bf16_f32 v4, v8, v9
	v_cvt_pk_bf16_f32 v5, v10, v11
	s_mov_b64 s[2:3], -1
	ds_write_b64 v234, v[4:5] offset:64
	s_cbranch_vccnz .LBB0_868
	global_load_dwordx4 v[4:7], v[22:23], off offset:576
	s_waitcnt vmcnt(0)
	s_mov_b64 s[2:3], 0
.LBB0_868:
	v_readlane_b32 s6, v250, 32
	s_andn2_b64 vcc, exec, s[2:3]
	v_readlane_b32 s7, v250, 33
	s_cbranch_vccnz .LBB0_870
	v_lshlrev_b32_e32 v4, 16, v232
	v_and_b32_e32 v5, 0xffff0000, v232
	v_lshlrev_b32_e32 v6, 16, v233
	v_and_b32_e32 v7, 0xffff0000, v233
.LBB0_870:
	v_mul_f32_e32 v13, v13, v13
	v_mul_f32_e32 v20, v25, v25
	v_mul_f32_e32 v19, v19, v19
	v_fmac_f32_e32 v13, v12, v12
	v_mul_f32_e32 v12, v15, v15
	v_mul_f32_e32 v9, v9, v9
	v_fmac_f32_e32 v20, v24, v24
	v_fmac_f32_e32 v19, v18, v18
	v_fmac_f32_e32 v12, v14, v14
	v_fmac_f32_e32 v9, v8, v8
	v_mul_f32_e32 v8, v11, v11
	v_pk_add_f32 v[2:3], v[2:3], v[6:7]
	v_pk_add_f32 v[4:5], v[0:1], v[4:5]
	v_add_f32_e32 v18, v20, v19
	v_add_f32_e32 v12, v13, v12
	v_fmac_f32_e32 v8, v10, v10
	v_mul_f32_e32 v0, v5, v5
	v_mul_f32_e32 v1, v3, v3
	v_add_f32_e32 v12, v18, v12
	v_add_f32_e32 v8, v9, v8
	v_fmac_f32_e32 v0, v4, v4
	v_fmac_f32_e32 v1, v2, v2
	v_add_f32_e32 v8, v12, v8
	v_add_f32_e32 v0, v0, v1
	v_add_f32_e32 v0, v8, v0
	ds_bpermute_b32 v1, v150, v0
	v_cvt_pk_bf16_f32 v4, v4, v5
	v_cvt_pk_bf16_f32 v5, v2, v3
	ds_write_b64 v234, v[4:5] offset:96
	s_waitcnt lgkmcnt(0)
	ds_read_b128 v[226:229], v235
	ds_read_b128 v[230:233], v235 offset:1152
	v_lshl_add_u64 v[238:239], v[16:17], 0, v[236:237]
	s_waitcnt lgkmcnt(1)
	global_store_dwordx4 v[238:239], v[226:229], off
	v_lshl_add_u64 v[238:239], v[238:239], 0, v[206:207]
	s_waitcnt lgkmcnt(0)
	global_store_dwordx4 v[238:239], v[230:233], off
	s_waitcnt lgkmcnt(0)
	v_add_f32_e32 v0, v0, v1
	ds_bpermute_b32 v1, v151, v0
	s_and_saveexec_b64 s[2:3], s[36:37]
	s_cbranch_execz .LBB0_872
	s_add_u32 s4, s6, s24
	s_addc_u32 s5, s7, s25
	v_lshl_add_u64 v[2:3], v[138:139], 2, s[4:5]
	s_waitcnt lgkmcnt(0)
	v_add_f32_e32 v0, v0, v1
	global_store_dword v[2:3], v0, off offset:704
